# attention loop: both wave groups raise s_setprio to 1 for the PV + row-max segment of each step and drop it at the step end (on top of the half-step stagger)
# speedup vs baseline: 1.0105x; 1.0105x over previous
; template <bool FIRST>
; __device__ __forceinline__ void partialSM(f32x16& p0, f32x16& p1, float& m_reg, f32x16& nm16, float& alpha) {
;   float pmax = p0[0];
; #pragma unroll
;   for (int r = 1; r < 16; ++r) pmax = fmaxf(pmax, p0[r]);
; #pragma unroll
;   for (int r = 0; r < 16; ++r) pmax = fmaxf(pmax, p1[r]);
;   { auto rr = __builtin_amdgcn_permlane32_swap(__float_as_uint(pmax), __float_as_uint(pmax), false, false);
;     pmax = fmaxf(__uint_as_float(rr[0]), __uint_as_float(rr[1])); }
;   if (!FIRST && __builtin_expect(__all(pmax <= THR2), 1)) { alpha = 1.f; }
; __device__ __forceinline__ void pv_d0(f32x16* o, const char* Vs, v8i pa, int r32, int hi) {
; #pragma unroll
;   for (int d0 = 0; d0 < 4; ++d0) { const int row = 32 * d0 + r32, x = (row >> 2) & 3;
;     const v8i vb = __builtin_shufflevector(*reinterpret_cast<const v4i*>(Vs + row * 64 + (((2 * hi) ^ x) << 4)), *reinterpret_cast<const v4i*>(Vs + row * 64 + (((2 * hi + 1) ^ x) << 4)), 0, 1, 2, 3, 4, 5, 6, 7);
;     o[d0] = __builtin_amdgcn_mfma_scale_f32_32x32x64_f8f6f4(pa, vb, o[d0], 0, 0, 0, 0, 0, 0); }
; }
.Lstg_mid0_l0:
	s_setprio 1
	v_add_u32_e32 v194, v204, v203
	v_add_u32_e32 v193, v204, v202
	ds_read_b128 v[86:89], v194
	ds_read_b128 v[82:85], v193
	ds_read_b128 v[90:93], v193 offset:2048
	ds_read_b128 v[94:97], v194 offset:2048
	s_nop 4
	v_max_f32_e32 v182, v114, v115
	v_max_f32_e32 v183, v114, v114
	s_waitcnt lgkmcnt(0)
	v_mfma_f32_32x32x64_f8f6f4 v[2:17], v[130:137], v[82:89], v[2:17]
	v_max3_f32 v182, v182, v116, v117
	v_max3_f32 v182, v182, v118, v119
	v_max3_f32 v182, v182, v120, v121
	v_max3_f32 v182, v182, v122, v123
	v_max3_f32 v182, v182, v124, v125
	v_max3_f32 v182, v182, v126, v127
	v_max3_f32 v182, v182, v128, v129
	v_max3_f32 v182, v182, v98, v99
	v_mov_b32_e32 v208, 1.0
	v_mfma_f32_32x32x64_f8f6f4 v[50:65], v[130:137], v[90:97], v[50:65]
	ds_read_b128 v[82:85], v193 offset:4096
	ds_read_b128 v[90:93], v193 offset:6144
	ds_read_b128 v[86:89], v194 offset:4096
	ds_read_b128 v[94:97], v194 offset:6144
	s_waitcnt lgkmcnt(0)
	v_mfma_f32_32x32x64_f8f6f4 v[34:49], v[130:137], v[82:89], v[34:49]
	v_max3_f32 v82, v182, v100, v101
	v_max3_f32 v82, v82, v102, v103
	v_max3_f32 v82, v82, v104, v105
	v_max3_f32 v82, v82, v106, v107
	v_max3_f32 v82, v82, v108, v109
	v_max3_f32 v82, v82, v110, v111
	v_max3_f32 v82, v82, v112, v113
	v_mov_b32_e32 v83, v82
	s_nop 1
	v_permlane32_swap_b32_e32 v82, v83
	v_max_f32_e32 v82, v82, v83
	v_cmp_ge_f32_e32 vcc, s85, v82
	s_cmp_eq_u64 vcc, exec
	v_mfma_f32_32x32x64_f8f6f4 v[18:33], v[130:137], v[90:97], v[18:33]
	s_cbranch_scc0 .LBB0_931
	s_setprio 0
	s_branch .LBB0_894

; template <bool FIRST>
; __device__ __forceinline__ void partialSM(f32x16& p0, f32x16& p1, float& m_reg, f32x16& nm16, float& alpha) {
;   float pmax = p0[0];
; #pragma unroll
;   for (int r = 1; r < 16; ++r) pmax = fmaxf(pmax, p0[r]);
; #pragma unroll
;   for (int r = 0; r < 16; ++r) pmax = fmaxf(pmax, p1[r]);
;   { auto rr = __builtin_amdgcn_permlane32_swap(__float_as_uint(pmax), __float_as_uint(pmax), false, false);
;     pmax = fmaxf(__uint_as_float(rr[0]), __uint_as_float(rr[1])); }
;   if (!FIRST && __builtin_expect(__all(pmax <= THR2), 1)) { alpha = 1.f; }
; __device__ __forceinline__ void pv_d0(f32x16* o, const char* Vs, v8i pa, int r32, int hi) {
; #pragma unroll
;   for (int d0 = 0; d0 < 4; ++d0) { const int row = 32 * d0 + r32, x = (row >> 2) & 3;
;     const v8i vb = __builtin_shufflevector(*reinterpret_cast<const v4i*>(Vs + row * 64 + (((2 * hi) ^ x) << 4)), *reinterpret_cast<const v4i*>(Vs + row * 64 + (((2 * hi + 1) ^ x) << 4)), 0, 1, 2, 3, 4, 5, 6, 7);
;     o[d0] = __builtin_amdgcn_mfma_scale_f32_32x32x64_f8f6f4(pa, vb, o[d0], 0, 0, 0, 0, 0, 0); }
; }
.Lstg_mid1_l0:
	s_setprio 1
	ds_read_b128 v[102:105], v194 offset:32768
	ds_read_b128 v[98:101], v193 offset:32768
	ds_read_b128 v[106:109], v193 offset:34816
	ds_read_b128 v[110:113], v194 offset:34816
	s_nop 6
	v_max_f32_e32 v182, v114, v115
	v_max_f32_e32 v183, v114, v114
	s_waitcnt lgkmcnt(0)
	v_mfma_f32_32x32x64_f8f6f4 v[2:17], v[130:137], v[98:105], v[2:17]
	v_max3_f32 v182, v182, v116, v117
	v_max3_f32 v182, v182, v118, v119
	v_max3_f32 v182, v182, v120, v121
	v_max3_f32 v182, v182, v122, v123
	v_max3_f32 v182, v182, v124, v125
	v_max3_f32 v182, v182, v126, v127
	v_max3_f32 v182, v182, v128, v129
	v_max3_f32 v182, v182, v82, v83
	v_mov_b32_e32 v211, 1.0
	v_mfma_f32_32x32x64_f8f6f4 v[50:65], v[130:137], v[106:113], v[50:65]
	ds_read_b128 v[98:101], v193 offset:36864
	ds_read_b128 v[106:109], v193 offset:38912
	ds_read_b128 v[102:105], v194 offset:36864
	ds_read_b128 v[110:113], v194 offset:38912
	s_waitcnt lgkmcnt(0)
	v_mfma_f32_32x32x64_f8f6f4 v[34:49], v[130:137], v[98:105], v[34:49]
	v_max3_f32 v98, v182, v84, v85
	v_max3_f32 v98, v98, v86, v87
	v_max3_f32 v98, v98, v88, v89
	v_max3_f32 v98, v98, v90, v91
	v_max3_f32 v98, v98, v92, v93
	v_max3_f32 v98, v98, v94, v95
	v_max3_f32 v98, v98, v96, v97
	v_mov_b32_e32 v99, v98
	s_nop 1
	v_permlane32_swap_b32_e32 v98, v99
	v_max_f32_e32 v98, v98, v99
	v_cmp_ge_f32_e32 vcc, s85, v98
	s_cmp_eq_u64 vcc, exec
	v_mfma_f32_32x32x64_f8f6f4 v[18:33], v[130:137], v[106:113], v[18:33]
	s_cbranch_scc0 .LBB0_932
	s_setprio 0
	s_branch .LBB0_901

; template <bool FIRST>
; __device__ __forceinline__ void partialSM(f32x16& p0, f32x16& p1, float& m_reg, f32x16& nm16, float& alpha) {
;   float pmax = p0[0];
; #pragma unroll
;   for (int r = 1; r < 16; ++r) pmax = fmaxf(pmax, p0[r]);
; #pragma unroll
;   for (int r = 0; r < 16; ++r) pmax = fmaxf(pmax, p1[r]);
;   { auto rr = __builtin_amdgcn_permlane32_swap(__float_as_uint(pmax), __float_as_uint(pmax), false, false);
;     pmax = fmaxf(__uint_as_float(rr[0]), __uint_as_float(rr[1])); }
;   if (!FIRST && __builtin_expect(__all(pmax <= THR2), 1)) { alpha = 1.f; }
; __device__ __forceinline__ void pv_d0(f32x16* o, const char* Vs, v8i pa, int r32, int hi) {
; #pragma unroll
;   for (int d0 = 0; d0 < 4; ++d0) { const int row = 32 * d0 + r32, x = (row >> 2) & 3;
;     const v8i vb = __builtin_shufflevector(*reinterpret_cast<const v4i*>(Vs + row * 64 + (((2 * hi) ^ x) << 4)), *reinterpret_cast<const v4i*>(Vs + row * 64 + (((2 * hi + 1) ^ x) << 4)), 0, 1, 2, 3, 4, 5, 6, 7);
;     o[d0] = __builtin_amdgcn_mfma_scale_f32_32x32x64_f8f6f4(pa, vb, o[d0], 0, 0, 0, 0, 0, 0); }
; }
.Lstg_mid2_l0:
	s_setprio 1
	ds_read_b128 v[86:89], v194 offset:40960
	ds_read_b128 v[82:85], v193 offset:40960
	ds_read_b128 v[90:93], v193 offset:43008
	ds_read_b128 v[94:97], v194 offset:43008
	v_max_f32_e32 v182, v114, v115
	v_max_f32_e32 v183, v114, v114
	s_waitcnt lgkmcnt(0)
	v_mfma_f32_32x32x64_f8f6f4 v[2:17], v[130:137], v[82:89], v[2:17]
	v_max3_f32 v182, v182, v116, v117
	v_max3_f32 v182, v182, v118, v119
	v_max3_f32 v182, v182, v120, v121
	v_max3_f32 v182, v182, v122, v123
	v_max3_f32 v182, v182, v124, v125
	v_max3_f32 v182, v182, v126, v127
	v_max3_f32 v182, v182, v128, v129
	v_max3_f32 v182, v182, v98, v99
	v_mov_b32_e32 v214, 1.0
	v_mfma_f32_32x32x64_f8f6f4 v[50:65], v[130:137], v[90:97], v[50:65]
	ds_read_b128 v[82:85], v193 offset:45056
	ds_read_b128 v[90:93], v193 offset:47104
	ds_read_b128 v[86:89], v194 offset:45056
	ds_read_b128 v[94:97], v194 offset:47104
	s_waitcnt lgkmcnt(0)
	v_mfma_f32_32x32x64_f8f6f4 v[34:49], v[130:137], v[82:89], v[34:49]
	v_max3_f32 v82, v182, v100, v101
	v_max3_f32 v82, v82, v102, v103
	v_max3_f32 v82, v82, v104, v105
	v_max3_f32 v82, v82, v106, v107
	v_max3_f32 v82, v82, v108, v109
	v_max3_f32 v82, v82, v110, v111
	v_max3_f32 v82, v82, v112, v113
	v_mov_b32_e32 v83, v82
	s_nop 1
	v_permlane32_swap_b32_e32 v82, v83
	v_max_f32_e32 v82, v82, v83
	v_cmp_ge_f32_e32 vcc, s85, v82
	s_cmp_eq_u64 vcc, exec
	v_mfma_f32_32x32x64_f8f6f4 v[18:33], v[130:137], v[90:97], v[18:33]
	s_cbranch_scc0 .LBB0_933
	s_setprio 0
	s_branch .LBB0_908

; template <bool FIRST>
; __device__ __forceinline__ void partialSM(f32x16& p0, f32x16& p1, float& m_reg, f32x16& nm16, float& alpha) {
;   float pmax = p0[0];
; #pragma unroll
;   for (int r = 1; r < 16; ++r) pmax = fmaxf(pmax, p0[r]);
; #pragma unroll
;   for (int r = 0; r < 16; ++r) pmax = fmaxf(pmax, p1[r]);
;   { auto rr = __builtin_amdgcn_permlane32_swap(__float_as_uint(pmax), __float_as_uint(pmax), false, false);
;     pmax = fmaxf(__uint_as_float(rr[0]), __uint_as_float(rr[1])); }
;   if (!FIRST && __builtin_expect(__all(pmax <= THR2), 1)) { alpha = 1.f; }
; __device__ __forceinline__ void pv_d0(f32x16* o, const char* Vs, v8i pa, int r32, int hi) {
; #pragma unroll
;   for (int d0 = 0; d0 < 4; ++d0) { const int row = 32 * d0 + r32, x = (row >> 2) & 3;
;     const v8i vb = __builtin_shufflevector(*reinterpret_cast<const v4i*>(Vs + row * 64 + (((2 * hi) ^ x) << 4)), *reinterpret_cast<const v4i*>(Vs + row * 64 + (((2 * hi + 1) ^ x) << 4)), 0, 1, 2, 3, 4, 5, 6, 7);
;     o[d0] = __builtin_amdgcn_mfma_scale_f32_32x32x64_f8f6f4(pa, vb, o[d0], 0, 0, 0, 0, 0, 0); }
; }
.Lstg_mid3_l0:
	s_setprio 1
	ds_read_b128 v[102:105], v194
	ds_read_b128 v[98:101], v193
	ds_read_b128 v[106:109], v193 offset:2048
	ds_read_b128 v[110:113], v194 offset:2048
	s_nop 6
	v_max_f32_e32 v182, v114, v115
	v_max_f32_e32 v183, v114, v114
	s_waitcnt lgkmcnt(0)
	v_mfma_f32_32x32x64_f8f6f4 v[2:17], v[130:137], v[98:105], v[2:17]
	v_max3_f32 v182, v182, v116, v117
	v_max3_f32 v182, v182, v118, v119
	v_max3_f32 v182, v182, v120, v121
	v_max3_f32 v182, v182, v122, v123
	v_max3_f32 v182, v182, v124, v125
	v_max3_f32 v182, v182, v126, v127
	v_max3_f32 v182, v182, v128, v129
	v_max3_f32 v182, v182, v82, v83
	v_mov_b32_e32 v217, 1.0
	v_mfma_f32_32x32x64_f8f6f4 v[50:65], v[130:137], v[106:113], v[50:65]
	ds_read_b128 v[98:101], v193 offset:4096
	ds_read_b128 v[106:109], v193 offset:6144
	ds_read_b128 v[102:105], v194 offset:4096
	ds_read_b128 v[110:113], v194 offset:6144
	s_waitcnt lgkmcnt(0)
	v_mfma_f32_32x32x64_f8f6f4 v[34:49], v[130:137], v[98:105], v[34:49]
	v_max3_f32 v98, v182, v84, v85
	v_max3_f32 v98, v98, v86, v87
	v_max3_f32 v98, v98, v88, v89
	v_max3_f32 v98, v98, v90, v91
	v_max3_f32 v98, v98, v92, v93
	v_max3_f32 v98, v98, v94, v95
	v_max3_f32 v98, v98, v96, v97
	v_mov_b32_e32 v99, v98
	s_nop 1
	v_permlane32_swap_b32_e32 v98, v99
	v_max_f32_e32 v98, v98, v99
	v_cmp_ge_f32_e32 vcc, s85, v98
	s_cmp_eq_u64 vcc, exec
	v_mfma_f32_32x32x64_f8f6f4 v[18:33], v[130:137], v[106:113], v[18:33]
	s_cbranch_scc0 .LBB0_934
	s_setprio 0
	s_branch .LBB0_915

; template <bool FIRST>
; __device__ __forceinline__ void partialSM(f32x16& p0, f32x16& p1, float& m_reg, f32x16& nm16, float& alpha) {
;   float pmax = p0[0];
; #pragma unroll
;   for (int r = 1; r < 16; ++r) pmax = fmaxf(pmax, p0[r]);
; #pragma unroll
;   for (int r = 0; r < 16; ++r) pmax = fmaxf(pmax, p1[r]);
;   { auto rr = __builtin_amdgcn_permlane32_swap(__float_as_uint(pmax), __float_as_uint(pmax), false, false);
;     pmax = fmaxf(__uint_as_float(rr[0]), __uint_as_float(rr[1])); }
;   if (!FIRST && __builtin_expect(__all(pmax <= THR2), 1)) { alpha = 1.f; }
; __device__ __forceinline__ void pv_d0(f32x16* o, const char* Vs, v8i pa, int r32, int hi) {
; #pragma unroll
;   for (int d0 = 0; d0 < 4; ++d0) { const int row = 32 * d0 + r32, x = (row >> 2) & 3;
;     const v8i vb = __builtin_shufflevector(*reinterpret_cast<const v4i*>(Vs + row * 64 + (((2 * hi) ^ x) << 4)), *reinterpret_cast<const v4i*>(Vs + row * 64 + (((2 * hi + 1) ^ x) << 4)), 0, 1, 2, 3, 4, 5, 6, 7);
;     o[d0] = __builtin_amdgcn_mfma_scale_f32_32x32x64_f8f6f4(pa, vb, o[d0], 0, 0, 0, 0, 0, 0); }
; }
.Lstg_mid4_l0:
	s_setprio 1
	ds_read_b128 v[86:89], v194 offset:32768
	ds_read_b128 v[82:85], v193 offset:32768
	ds_read_b128 v[90:93], v193 offset:34816
	ds_read_b128 v[94:97], v194 offset:34816
	v_max_f32_e32 v182, v114, v115
	v_max_f32_e32 v183, v114, v114
	s_waitcnt lgkmcnt(0)
	v_mfma_f32_32x32x64_f8f6f4 v[2:17], v[130:137], v[82:89], v[2:17]
	v_max3_f32 v182, v182, v116, v117
	v_max3_f32 v182, v182, v118, v119
	v_max3_f32 v182, v182, v120, v121
	v_max3_f32 v182, v182, v122, v123
	v_max3_f32 v182, v182, v124, v125
	v_max3_f32 v182, v182, v126, v127
	v_max3_f32 v182, v182, v128, v129
	v_max3_f32 v182, v182, v98, v99
	v_mov_b32_e32 v220, 1.0
	v_mfma_f32_32x32x64_f8f6f4 v[50:65], v[130:137], v[90:97], v[50:65]
	ds_read_b128 v[82:85], v193 offset:36864
	ds_read_b128 v[90:93], v193 offset:38912
	ds_read_b128 v[86:89], v194 offset:36864
	ds_read_b128 v[94:97], v194 offset:38912
	s_waitcnt lgkmcnt(0)
	v_mfma_f32_32x32x64_f8f6f4 v[34:49], v[130:137], v[82:89], v[34:49]
	v_max3_f32 v82, v182, v100, v101
	v_max3_f32 v82, v82, v102, v103
	v_max3_f32 v82, v82, v104, v105
	v_max3_f32 v82, v82, v106, v107
	v_max3_f32 v82, v82, v108, v109
	v_max3_f32 v82, v82, v110, v111
	v_max3_f32 v82, v82, v112, v113
	v_mov_b32_e32 v83, v82
	s_nop 1
	v_permlane32_swap_b32_e32 v82, v83
	v_max_f32_e32 v82, v82, v83
	v_cmp_ge_f32_e32 vcc, s85, v82
	s_cmp_eq_u64 vcc, exec
	v_mfma_f32_32x32x64_f8f6f4 v[18:33], v[130:137], v[90:97], v[18:33]
	s_cbranch_scc0 .LBB0_935
	s_setprio 0
	s_branch .LBB0_922

; template <bool FIRST>
; __device__ __forceinline__ void partialSM(f32x16& p0, f32x16& p1, float& m_reg, f32x16& nm16, float& alpha) {
;   float pmax = p0[0];
; #pragma unroll
;   for (int r = 1; r < 16; ++r) pmax = fmaxf(pmax, p0[r]);
; #pragma unroll
;   for (int r = 0; r < 16; ++r) pmax = fmaxf(pmax, p1[r]);
;   { auto rr = __builtin_amdgcn_permlane32_swap(__float_as_uint(pmax), __float_as_uint(pmax), false, false);
;     pmax = fmaxf(__uint_as_float(rr[0]), __uint_as_float(rr[1])); }
;   if (!FIRST && __builtin_expect(__all(pmax <= THR2), 1)) { alpha = 1.f; }
; __device__ __forceinline__ void pv_d0(f32x16* o, const char* Vs, v8i pa, int r32, int hi) {
; #pragma unroll
;   for (int d0 = 0; d0 < 4; ++d0) { const int row = 32 * d0 + r32, x = (row >> 2) & 3;
;     const v8i vb = __builtin_shufflevector(*reinterpret_cast<const v4i*>(Vs + row * 64 + (((2 * hi) ^ x) << 4)), *reinterpret_cast<const v4i*>(Vs + row * 64 + (((2 * hi + 1) ^ x) << 4)), 0, 1, 2, 3, 4, 5, 6, 7);
;     o[d0] = __builtin_amdgcn_mfma_scale_f32_32x32x64_f8f6f4(pa, vb, o[d0], 0, 0, 0, 0, 0, 0); }
; }
.Lstg_mid5_l0:
	s_setprio 1
	ds_read_b128 v[104:107], v194 offset:40960
	ds_read_b128 v[100:103], v193 offset:40960
	ds_read_b128 v[222:225], v193 offset:43008
	ds_read_b128 v[226:229], v194 offset:43008
	v_max_f32_e32 v108, v114, v115
	v_max_f32_e32 v109, v114, v114
	s_waitcnt lgkmcnt(0)
	v_mfma_f32_32x32x64_f8f6f4 v[2:17], v[130:137], v[100:107], v[2:17]
	v_max3_f32 v108, v108, v116, v117
	v_max3_f32 v108, v108, v118, v119
	v_max3_f32 v108, v108, v120, v121
	v_max3_f32 v108, v108, v122, v123
	v_max3_f32 v108, v108, v124, v125
	v_max3_f32 v108, v108, v126, v127
	v_max3_f32 v108, v108, v128, v129
	v_max3_f32 v108, v108, v82, v83
	v_mov_b32_e32 v176, 1.0
	v_mfma_f32_32x32x64_f8f6f4 v[50:65], v[130:137], v[222:229], v[50:65]
	ds_read_b128 v[100:103], v193 offset:45056
	ds_read_b128 v[222:225], v193 offset:47104
	ds_read_b128 v[104:107], v194 offset:45056
	ds_read_b128 v[226:229], v194 offset:47104
	s_waitcnt lgkmcnt(0)
	v_mfma_f32_32x32x64_f8f6f4 v[34:49], v[130:137], v[100:107], v[34:49]
	v_max3_f32 v100, v108, v84, v85
	v_max3_f32 v100, v100, v86, v87
	v_max3_f32 v100, v100, v88, v89
	v_max3_f32 v100, v100, v90, v91
	v_max3_f32 v100, v100, v92, v93
	v_max3_f32 v100, v100, v94, v95
	v_max3_f32 v100, v100, v96, v97
	v_mov_b32_e32 v101, v100
	s_nop 1
	v_permlane32_swap_b32_e32 v100, v101
	v_max_f32_e32 v100, v100, v101
	v_cmp_ge_f32_e32 vcc, s85, v100
	s_cmp_eq_u64 vcc, exec
	v_mfma_f32_32x32x64_f8f6f4 v[18:33], v[130:137], v[222:229], v[18:33]
	s_cbranch_scc0 .LBB0_936
	s_setprio 0
	s_branch .LBB0_929
